# v47 plus static s_setprio 1 for waves 4-7 during the MLA attention unit
# speedup vs baseline: 1.0226x; 1.0032x over previous
;     ...
;     int tid = tid_x(); asm volatile("" : "+v"(tid));
;     const int wid = tid >> 6, lane = tid & 63, r32 = lane & 31, hi = lane >> 5;
;     const int qb = uid & 15, h = (uid >> 4) % NH, b = (uid >> 4) / NH;
;     const int tok0 = b * SEQ;
;     const int qrow = tok0 + qb * 256 + wid * 32 + r32;
;     LAS char* V_lds = lds + LDS_VBUF; LAS char* K_lds = lds + LDS_KBUF;
;     LAS float* ws = (LAS float*)(lds + LDS_WS) + wid * 64; LAS float* li_l = ws; LAS float* al_l = ws + 32;
;     LAS float* rpbL = (LAS float*)(lds + LDS_RPB);
;     const int sr = tid >> 4, sc = (tid & 15) * 8, vst0 = v_st(sr, sc), vst1 = v_st(32 + sr, sc);
;     const int sr64 = tid >> 3, sc64 = (tid & 7) * 8;
;     const int vb0 = (int)(unsigned)(uintptr_t)V_lds + v_rd_base(lane);
;     int NT = 64, kbase = tok0;
;     int rq = 0, qc = 0, kr_lo = 0;
;     if constexpr (MODE == MODE_NA) { const int rq0 = qb * 4; kr_lo = min(min(max(rq0 - 4, 0), 56), 52); NT = 12; kbase = tok0 + kr_lo * 64; rq = rq0 + (wid >> 1); qc = (wid & 1) * 32 + r32;
;         for (int i = tid; i < 15 * 31; i += 512) rpbL[i] = P.rpb[h * 465 + i];
;         __syncthreads(); }
;     const bf16* Kg; const bf16* Vg; const bf16* Kg2 = nullptr; int ldk, ldv;
;     if constexpr (MODE == MODE_MLA) { Kg = P.KVM + h * 256; Vg = P.KVM + h * 256 + 128; Kg2 = P.U + U_KR; ldk = KVW; ldv = KVW; }
;     else if constexpr (MODE == MODE_NA) { Kg = P.U + U_NA + 512 + h * 128; Vg = P.U + U_NA + 1024 + h * 128; ldk = UW; ldv = UW; }
;     else { Kg = P.U + U_DF + 512 + h * 128; Vg = P.U + U_DF + 1024 + h * 128; ldk = UW; ldv = UW; }
;     constexpr int pass = PASS;
;     constexpr bool HALF_OFFSET = false;
;     {
;         float m_reg = -1e30f, l_reg = 0; f32x16 o[4] = {}; bf16x8 qr[NQ];
;         if constexpr (MODE == MODE_MLA) {
;             const bf16* Qw = P.QM + (size_t)qrow * QMW + h * 192 + hi * 8;
; #pragma unroll
;             for (int d0 = 0; d0 < 12; ++d0) qr[d0] = *(const bf16x8*)(Qw + d0 * 16);
;             const f32x2* rt = P.ropeM + (size_t)(qrow & (SEQ - 1)) * 32;
; #pragma unroll
;             for (int g = 0; g < 2; ++g) {
;                 bf16x8 x1 = qr[8 + g], x2 = qr[10 + g];
; #pragma unroll
;                 for (int e = 0; e < 8; ++e) { const f32x2 cs = rt[g * 16 + hi * 8 + e];
;                     const float a = bf2f((unsigned short)x1[e]), c = bf2f((unsigned short)x2[e]);
.LBB0_785:
	s_lshl_b32 s0, s22, 1
	s_and_b32 s0, s0, 14
	s_ashr_i32 s1, s22, 7
	s_add_i32 s0, s0, s1
	s_getreg_b32 s1, hwreg(HW_REG_HW_ID, 0, 6)
	s_and_b32 s1, s1, 63
	s_lshl_b32 s1, s1, 2
	s_add_i32 s1, s1, 0
	s_add_i32 s1, s1, 0x23f00
	s_waitcnt vmcnt(15)
	v_mov_b32_e32 v0, s1
	ds_read_b32 v0, v0
	v_mbcnt_lo_u32_b32 v1, -1, 0
	v_mbcnt_hi_u32_b32 v1, -1, v1
	v_mov_b32_e32 v145, v193
	v_mov_b32_e32 v149, v193
	s_movk_i32 s3, 0x70
	s_waitcnt lgkmcnt(0)
	v_readfirstlane_b32 s1, v0
	s_mov_b32 s28, 0
	s_cmp_ge_u32 s1, 4
	s_cbranch_scc0 .Lprio_mla_skip
	s_setprio 1
.Lprio_mla_skip:
	v_mov_b32_e32 v147, v193
	s_waitcnt vmcnt(13)
	v_lshl_add_u32 v11, s1, 6, v1
	s_lshr_b32 s1, s0, 29
	s_add_i32 s1, s0, s1
	s_and_b32 s2, s1, -8
	s_sub_i32 s23, s0, s2
	s_lshl_b32 s0, s1, 9
	s_and_b32 s4, s0, 0xfffff000
	s_lshl_b32 s0, s22, 5
	s_and_b32 s0, s0, 0xf00
	s_or_b32 s25, s4, s0
	v_ashrrev_i32_e32 v156, 6, v11
	v_and_b32_e32 v154, 31, v11
	v_lshl_add_u32 v0, v156, 5, s25
	v_or_b32_e32 v8, v0, v154
	v_and_b32_e32 v0, 0x3fffffc0, v11
	s_add_i32 s0, 0, 0x1e000
	v_lshl_add_u32 v157, v0, 2, s0
	s_lshl_b32 s0, s23, 8
	s_ashr_i32 s1, s0, 31
	s_lshl_b64 s[0:1], s[0:1], 1
	s_add_u32 s26, s18, s0
	v_mov_b64_e32 v[0:1], s[10:11]
	s_movk_i32 s0, 0xc00
	s_addc_u32 s27, s19, s1
	v_mad_i64_i32 v[0:1], s[0:1], v8, s0, v[0:1]
	s_mul_i32 s0, s23, 0xc0
	v_lshlrev_b32_e32 v8, 8, v8
	v_bfe_u32 v155, v11, 5, 1
	s_ashr_i32 s1, s0, 31
	v_and_b32_e32 v192, 0xfff00, v8
	v_lshl_add_u64 v[0:1], s[0:1], 1, v[0:1]
	v_lshlrev_b32_e32 v144, 4, v155
	v_lshl_add_u64 v[8:9], s[12:13], 0, v[192:193]
	v_lshlrev_b32_e32 v192, 6, v155
	v_lshl_add_u64 v[4:5], v[0:1], 0, v[144:145]
	v_lshl_add_u64 v[8:9], v[8:9], 0, v[192:193]
	global_load_dwordx4 v[96:99], v[4:5], off
	global_load_dwordx4 v[100:103], v[4:5], off offset:32
	global_load_dwordx4 v[104:107], v[4:5], off offset:64
	global_load_dwordx4 v[108:111], v[4:5], off offset:96
	global_load_dwordx4 v[112:115], v[4:5], off offset:128
	global_load_dwordx4 v[116:119], v[4:5], off offset:160
	global_load_dwordx4 v[120:123], v[4:5], off offset:192
	global_load_dwordx4 v[124:127], v[4:5], off offset:224
	global_load_dwordx4 v[26:29], v[4:5], off offset:256
	global_load_dwordx4 v[0:3], v[4:5], off offset:288
	global_load_dwordx4 v[30:33], v[4:5], off offset:320
	s_nop 0
	global_load_dwordx4 v[4:7], v[4:5], off offset:352
	s_waitcnt vmcnt(24)
	v_lshlrev_b32_e32 v13, 4, v11
	global_load_dwordx2 v[14:15], v[8:9], off
	v_readfirstlane_b32 s0, v156
	s_ashr_i32 s5, s4, 31
	s_lshl_b32 s2, s0, 10
	s_lshl_b64 s[0:1], s[4:5], 12
	s_add_u32 s0, s26, s0
	s_addc_u32 s1, s27, s1
	s_add_i32 s29, s2, 0
	s_mov_b32 m0, s29
	s_add_i32 s2, s29, 0xc000
	v_and_b32_e32 v10, 63, v11
	v_and_b32_e32 v12, 0xc0, v13
	v_mov_b32_e32 v151, v193
	v_lshlrev_b32_e32 v145, 8, v154
	v_lshlrev_b32_e32 v167, 7, v154
	v_lshl_add_u32 v163, v154, 2, v157
	v_mov_b32_e32 v174, 0
	v_mov_b32_e32 v173, 0xf149f2ca
	s_waitcnt vmcnt(4)
	v_lshlrev_b32_e32 v17, 16, v26
	s_waitcnt vmcnt(2)
	v_lshlrev_b32_e32 v16, 16, v30
	s_waitcnt vmcnt(0)
	v_pk_mul_f32 v[18:19], v[14:15], v[16:17] op_sel:[0,1] op_sel_hi:[1,0]
	v_pk_mul_f32 v[14:15], v[14:15], v[16:17]
	v_sub_f32_e32 v18, v18, v19
	v_add_f32_e32 v14, v15, v14
	v_cvt_pk_bf16_f32 v15, v18, v193
	v_cvt_pk_bf16_f32 v14, v14, v193
	global_load_dwordx2 v[16:17], v[8:9], off offset:8
	v_and_b32_e32 v19, 0xffff0000, v26
	v_and_b32_e32 v18, 0xffff0000, v30
	s_waitcnt vmcnt(0)
	v_pk_mul_f32 v[20:21], v[16:17], v[18:19] op_sel:[0,1] op_sel_hi:[1,0]
	v_pk_mul_f32 v[16:17], v[16:17], v[18:19]
	v_sub_f32_e32 v20, v20, v21
	v_add_f32_e32 v16, v16, v17
	v_cvt_pk_bf16_f32 v17, v20, v193
	v_cvt_pk_bf16_f32 v16, v16, v193
	global_load_dwordx2 v[18:19], v[8:9], off offset:16
	v_lshlrev_b32_e32 v21, 16, v27
	v_lshlrev_b32_e32 v20, 16, v31
	s_waitcnt vmcnt(0)
	v_pk_mul_f32 v[22:23], v[18:19], v[20:21] op_sel:[0,1] op_sel_hi:[1,0]
	v_pk_mul_f32 v[18:19], v[18:19], v[20:21]
	v_sub_f32_e32 v22, v22, v23
	v_add_f32_e32 v18, v18, v19
	v_cvt_pk_bf16_f32 v19, v22, v193
	v_cvt_pk_bf16_f32 v18, v18, v193
	global_load_dwordx2 v[20:21], v[8:9], off offset:24
	v_and_b32_e32 v23, 0xffff0000, v27
	v_and_b32_e32 v22, 0xffff0000, v31
	s_waitcnt vmcnt(0)
	v_pk_mul_f32 v[24:25], v[20:21], v[22:23] op_sel:[0,1] op_sel_hi:[1,0]
	v_pk_mul_f32 v[20:21], v[20:21], v[22:23]
	v_sub_f32_e32 v24, v24, v25
	v_add_f32_e32 v20, v20, v21
	v_cvt_pk_bf16_f32 v21, v24, v193
	v_cvt_pk_bf16_f32 v20, v20, v193
	global_load_dwordx2 v[22:23], v[8:9], off offset:32
	v_lshlrev_b32_e32 v25, 16, v28
	v_lshlrev_b32_e32 v24, 16, v32
	s_waitcnt vmcnt(0)
	v_pk_mul_f32 v[26:27], v[22:23], v[24:25] op_sel:[0,1] op_sel_hi:[1,0]
	v_pk_mul_f32 v[22:23], v[22:23], v[24:25]
	v_sub_f32_e32 v26, v26, v27
	v_add_f32_e32 v22, v22, v23
	v_cvt_pk_bf16_f32 v23, v26, v193
	v_cvt_pk_bf16_f32 v22, v22, v193
	global_load_dwordx2 v[24:25], v[8:9], off offset:40
	v_and_b32_e32 v27, 0xffff0000, v28
	v_and_b32_e32 v26, 0xffff0000, v32
	s_waitcnt vmcnt(0)
	v_pk_mul_f32 v[30:31], v[24:25], v[26:27] op_sel:[0,1] op_sel_hi:[1,0]
	v_pk_mul_f32 v[24:25], v[24:25], v[26:27]
	v_sub_f32_e32 v28, v30, v31
	v_add_f32_e32 v24, v24, v25
	v_cvt_pk_bf16_f32 v25, v28, v193
	v_cvt_pk_bf16_f32 v24, v24, v193
	global_load_dwordx2 v[26:27], v[8:9], off offset:48
	v_lshlrev_b32_e32 v31, 16, v29
	v_lshlrev_b32_e32 v30, 16, v33
	v_and_b32_e32 v29, 0xffff0000, v29
	s_waitcnt vmcnt(0)
	v_pk_mul_f32 v[34:35], v[26:27], v[30:31] op_sel:[0,1] op_sel_hi:[1,0]
	v_pk_mul_f32 v[26:27], v[26:27], v[30:31]
	v_sub_f32_e32 v28, v34, v35
	v_add_f32_e32 v26, v26, v27
	v_cvt_pk_bf16_f32 v27, v28, v193
	v_cvt_pk_bf16_f32 v26, v26, v193
	global_load_dwordx2 v[30:31], v[8:9], off offset:56
	v_and_b32_e32 v28, 0xffff0000, v33
	v_lshlrev_b32_e32 v35, 16, v0
	v_lshlrev_b32_e32 v34, 16, v4
	s_waitcnt vmcnt(0)
; __device__ __forceinline__ unsigned cvt_pk_bf16(float lo, float hi) { unsigned r; asm volatile("v_cvt_pk_bf16_f32 %0, %1, %2" : "=v"(r) : "v"(lo), "v"(hi)); return r; }
;     ...
; #pragma unroll
;             for (int g = 0; g < 2; ++g) {
;                 bf16x8 x1 = qr[8 + g], x2 = qr[10 + g];
; #pragma unroll
;                 for (int e = 0; e < 8; ++e) { const f32x2 cs = rt[g * 16 + hi * 8 + e];
;                     const float a = bf2f((unsigned short)x1[e]), c = bf2f((unsigned short)x2[e]);
;                     const float ra = a * cs.x - c * cs.y, rc = c * cs.x + a * cs.y;
;                     x1[e] = (short)(cvt_pk_bf16(ra, 0.f) & 0xffffu); x2[e] = (short)(cvt_pk_bf16(rc, 0.f) & 0xffffu); }
;                 qr[8 + g] = x1; qr[10 + g] = x2;
;             }
	v_pk_mul_f32 v[32:33], v[30:31], v[28:29] op_sel:[0,1] op_sel_hi:[1,0]
	v_pk_mul_f32 v[28:29], v[30:31], v[28:29]
	v_sub_f32_e32 v32, v32, v33
	v_add_f32_e32 v28, v28, v29
	v_cvt_pk_bf16_f32 v30, v32, v193
	v_cvt_pk_bf16_f32 v28, v28, v193
	global_load_dwordx2 v[32:33], v[8:9], off offset:128
	s_waitcnt vmcnt(0)
	v_pk_mul_f32 v[36:37], v[32:33], v[34:35] op_sel:[0,1] op_sel_hi:[1,0]
	v_pk_mul_f32 v[32:33], v[32:33], v[34:35]
	v_sub_f32_e32 v29, v36, v37
	v_add_f32_e32 v32, v32, v33
	v_cvt_pk_bf16_f32 v31, v29, v193
	v_cvt_pk_bf16_f32 v29, v32, v193
	global_load_dwordx2 v[32:33], v[8:9], off offset:136
	v_and_b32_e32 v35, 0xffff0000, v0
	v_and_b32_e32 v34, 0xffff0000, v4
	s_waitcnt vmcnt(0)
	v_pk_mul_f32 v[36:37], v[32:33], v[34:35] op_sel:[0,1] op_sel_hi:[1,0]
	v_pk_mul_f32 v[32:33], v[32:33], v[34:35]
	v_sub_f32_e32 v0, v36, v37
	v_add_f32_e32 v4, v32, v33
	v_cvt_pk_bf16_f32 v32, v0, v193
	v_cvt_pk_bf16_f32 v4, v4, v193
	global_load_dwordx2 v[34:35], v[8:9], off offset:144
	v_lshlrev_b32_e32 v37, 16, v1
	v_lshlrev_b32_e32 v36, 16, v5
	v_and_b32_e32 v1, 0xffff0000, v1
	s_waitcnt vmcnt(0)
	v_pk_mul_f32 v[38:39], v[34:35], v[36:37] op_sel:[0,1] op_sel_hi:[1,0]
	v_pk_mul_f32 v[34:35], v[34:35], v[36:37]
	v_sub_f32_e32 v0, v38, v39
	v_add_f32_e32 v33, v34, v35
	v_cvt_pk_bf16_f32 v34, v0, v193
	v_cvt_pk_bf16_f32 v33, v33, v193
	global_load_dwordx2 v[36:37], v[8:9], off offset:152
	v_and_b32_e32 v0, 0xffff0000, v5
	s_waitcnt vmcnt(0)
	v_pk_mul_f32 v[38:39], v[36:37], v[0:1] op_sel:[0,1] op_sel_hi:[1,0]
	v_pk_mul_f32 v[0:1], v[36:37], v[0:1]
	v_sub_f32_e32 v5, v38, v39
	v_add_f32_e32 v0, v0, v1
	v_cvt_pk_bf16_f32 v35, v5, v193
	v_cvt_pk_bf16_f32 v5, v0, v193
	global_load_dwordx2 v[0:1], v[8:9], off offset:160
	v_lshlrev_b32_e32 v37, 16, v2
	v_lshlrev_b32_e32 v36, 16, v6
	s_waitcnt vmcnt(0)
	v_pk_mul_f32 v[38:39], v[0:1], v[36:37] op_sel:[0,1] op_sel_hi:[1,0]
	v_pk_mul_f32 v[0:1], v[0:1], v[36:37]
	v_sub_f32_e32 v38, v38, v39
	v_add_f32_e32 v0, v0, v1
	v_cvt_pk_bf16_f32 v37, v38, v193
	v_cvt_pk_bf16_f32 v36, v0, v193
	global_load_dwordx2 v[0:1], v[8:9], off offset:168
	v_and_b32_e32 v39, 0xffff0000, v2
	v_and_b32_e32 v38, 0xffff0000, v6
	s_waitcnt vmcnt(0)
	v_pk_mul_f32 v[40:41], v[0:1], v[38:39] op_sel:[0,1] op_sel_hi:[1,0]
	v_pk_mul_f32 v[0:1], v[0:1], v[38:39]
	v_sub_f32_e32 v2, v40, v41
	v_add_f32_e32 v0, v0, v1
	v_cvt_pk_bf16_f32 v6, v2, v193
	v_cvt_pk_bf16_f32 v2, v0, v193
	global_load_dwordx2 v[0:1], v[8:9], off offset:176
	v_lshlrev_b32_e32 v39, 16, v3
	v_lshlrev_b32_e32 v38, 16, v7
	s_waitcnt vmcnt(0)
	v_pk_mul_f32 v[40:41], v[0:1], v[38:39] op_sel:[0,1] op_sel_hi:[1,0]
	v_pk_mul_f32 v[0:1], v[0:1], v[38:39]
	v_sub_f32_e32 v40, v40, v41
	v_add_f32_e32 v0, v0, v1
	v_cvt_pk_bf16_f32 v39, v40, v193
	v_cvt_pk_bf16_f32 v38, v0, v193
	global_load_dwordx2 v[0:1], v[8:9], off offset:184
	v_and_b32_e32 v9, 0xffff0000, v3
	v_and_b32_e32 v8, 0xffff0000, v7
	s_waitcnt vmcnt(0)
; #define VM_WAIT() asm volatile("s_waitcnt vmcnt(0)" ::: "memory")
; __device__ __forceinline__ unsigned cvt_pk_bf16(float lo, float hi) { unsigned r; asm volatile("v_cvt_pk_bf16_f32 %0, %1, %2" : "=v"(r) : "v"(lo), "v"(hi)); return r; }
;     ...
;                 bf16x8 x1 = qr[8 + g], x2 = qr[10 + g];
; #pragma unroll
;                 for (int e = 0; e < 8; ++e) { const f32x2 cs = rt[g * 16 + hi * 8 + e];
;                     const float a = bf2f((unsigned short)x1[e]), c = bf2f((unsigned short)x2[e]);
;                     const float ra = a * cs.x - c * cs.y, rc = c * cs.x + a * cs.y;
;                     x1[e] = (short)(cvt_pk_bf16(ra, 0.f) & 0xffffu); x2[e] = (short)(cvt_pk_bf16(rc, 0.f) & 0xffffu); }
;                 qr[8 + g] = x1; qr[10 + g] = x2;
;             }
;     ...
;         unsigned gsv[2], gsk[2], gsk2 = 0u;
; #pragma unroll
;         for (int i = 0; i < 2; ++i) { const int a = (i * 512 + tid) * 16;
;             { const int sub = a >> 9, within = a & 511; const int kk = (sub >> 2) * 8 + (within >> 6); const int k = (kk & ~0xC) | ((kk & 4) << 1) | ((kk & 8) >> 1);
;               const int c = (sub & 3) * 32 + ((within & 63) >> 1); gsv[i] = (unsigned)(k * ldv + c) * 2u; }
;             if constexpr (MODE == MODE_DIFF) { if (i == 0) { const int row = a >> 7, ch = ((a >> 4) & 7) ^ ((row >> 1) & 7); gsk[0] = (unsigned)(row * ldk + ch * 8) * 2u; } gsk[1] = 0u; }
;             else { const int row = a >> 8, ch = ((a >> 4) & 15) ^ (row & 15); gsk[i] = (unsigned)(row * ldk + ch * 8) * 2u; } }
;         if constexpr (MODE == MODE_MLA) { const int a = tid * 16, row = a >> 7, ch = ((a >> 4) & 7) ^ ((row >> 1) & 7); gsk2 = (unsigned)(row * UW + ch * 8) * 2u; }
;         const unsigned ldsw = (unsigned)__builtin_amdgcn_readfirstlane(wid) * 1024u;
;     ...
;         GLDS(0, 0); VM_WAIT(); __syncthreads();
	v_pk_mul_f32 v[40:41], v[0:1], v[8:9] op_sel:[0,1] op_sel_hi:[1,0]
	v_pk_mul_f32 v[0:1], v[0:1], v[8:9]
	v_sub_f32_e32 v3, v40, v41
	v_add_f32_e32 v0, v0, v1
	v_bfe_i32 v9, v11, 4, 24
	v_cvt_pk_bf16_f32 v8, v3, v193
	v_cvt_pk_bf16_f32 v7, v0, v193
	v_bfe_u32 v0, v11, 2, 2
	v_lshrrev_b32_e32 v1, 1, v11
	v_lshlrev_b32_e32 v3, 1, v11
	v_lshrrev_b32_e32 v41, 1, v9
	v_and_or_b32 v0, v1, 8, v0
	v_and_b32_e32 v1, 0xc0, v3
	v_and_b32_e32 v40, 0xffff0, v9
	v_and_b32_e32 v41, 4, v41
	v_and_or_b32 v1, v13, 48, v1
	v_or3_b32 v40, v40, v41, v0
	v_lshl_or_b32 v192, v40, 12, v1
	v_xor_b32_e32 v40, v9, v11
	v_lshlrev_b32_e32 v9, 12, v9
	v_lshlrev_b32_e32 v40, 4, v40
	v_and_or_b32 v146, v40, s87, v9
	v_add_u32_e32 v9, 0x2000, v13
	v_ashrrev_i32_e32 v9, 8, v9
	v_lshrrev_b32_e32 v41, 1, v9
	v_and_b32_e32 v40, 0xffff0, v9
	v_and_b32_e32 v41, 4, v41
	v_or3_b32 v0, v40, v41, v0
	v_lshl_add_u64 v[40:41], s[0:1], 0, v[192:193]
	v_lshl_or_b32 v148, v0, 12, v1
	v_lshl_add_u64 v[40:41], v[40:41], 0, s[36:37]
	global_load_lds_dwordx4 v[40:41], off
	v_lshl_add_u64 v[40:41], s[0:1], 0, v[148:149]
	v_xor_b32_e32 v0, v9, v11
	v_lshl_add_u64 v[40:41], v[40:41], 0, s[36:37]
	s_add_i32 m0, s29, 0x2000
	v_lshlrev_b32_e32 v1, 12, v9
	v_lshlrev_b32_e32 v0, 4, v0
	global_load_lds_dwordx4 v[40:41], off
	s_mov_b32 m0, s2
	v_and_or_b32 v150, v0, s87, v1
	global_load_lds_dwordx4 v146, s[0:1]
	s_add_i32 m0, s29, 0xe000
	v_lshlrev_b32_e32 v0, 10, v11
	global_load_lds_dwordx4 v150, s[0:1]
	s_lshl_b64 s[0:1], s[4:5], 13
	v_and_b32_e32 v0, 0xffffe000, v0
	v_xor_b32_e32 v1, v13, v11
	s_add_u32 s0, s14, s0
	v_and_or_b32 v0, v1, s3, v0
	s_addc_u32 s1, s15, s1
	s_add_i32 m0, s29, 0x10000
	v_mov_b32_e32 v1, v193
	global_load_lds_dwordx4 v0, s[0:1]
	v_lshl_add_u64 v[152:153], s[14:15], 0, v[0:1]
	v_bitop3_b32 v0, v155, v11, 15 bitop3:0x78
	v_lshlrev_b32_e32 v9, 3, v11
	v_lshlrev_b32_e32 v158, 4, v0
	v_and_b32_e32 v0, 0xf0, v13
	v_bitop3_b32 v159, v144, v0, 32 bitop3:0x36
	v_bitop3_b32 v160, v144, v0, 64 bitop3:0x36
	v_bitop3_b32 v161, v144, v0, s60 bitop3:0x36
	v_bitop3_b32 v162, v144, v0, s59 bitop3:0x36
	v_bitop3_b32 v164, v144, v0, s61 bitop3:0x36
	v_bitop3_b32 v165, v144, v0, s58 bitop3:0x36
	v_bitop3_b32 v166, v144, v0, s62 bitop3:0x36
	v_and_b32_e32 v0, 0x70, v9
	v_bitop3_b32 v169, v144, v0, 32 bitop3:0x36
	v_bitop3_b32 v170, v144, v0, 64 bitop3:0x36
	v_bitop3_b32 v171, v144, v0, s60 bitop3:0x36
	v_and_b32_e32 v0, 0x118, v9
	s_mov_b32 s0, 0x5040100
	s_waitcnt vmcnt(0)
	v_perm_b32 v128, v17, v15, s0
	v_perm_b32 v136, v16, v14, s0
	v_and_or_b32 v0, v3, 32, v0
	v_mov_b32_e32 v14, v193
	v_mov_b32_e32 v15, v193
	v_bitop3_b32 v168, v144, v9, s3 bitop3:0x78
	v_cmp_gt_u32_e64 s[2:3], 32, v10
	v_perm_b32 v129, v21, v19, s0
	v_perm_b32 v130, v25, v23, s0
	v_perm_b32 v131, v30, v27, s0
	v_perm_b32 v132, v32, v31, s0
	v_perm_b32 v133, v35, v34, s0
	v_perm_b32 v134, v6, v37, s0
	v_perm_b32 v135, v8, v39, s0
	v_perm_b32 v137, v20, v18, s0
	v_perm_b32 v138, v24, v22, s0
	v_perm_b32 v139, v28, v26, s0
	v_perm_b32 v140, v4, v29, s0
	v_perm_b32 v141, v5, v33, s0
	v_perm_b32 v142, v2, v36, s0
	v_perm_b32 v143, v7, v38, s0
	v_add3_u32 v172, v12, 0, v0
	v_mov_b32_e32 v0, v193
	v_mov_b32_e32 v2, v193
	v_mov_b32_e32 v3, v193
	v_mov_b32_e32 v4, v193
	v_mov_b32_e32 v5, v193
	v_mov_b32_e32 v6, v193
	v_mov_b32_e32 v7, v193
	v_mov_b32_e32 v8, v193
	v_mov_b32_e32 v9, v193
	v_mov_b32_e32 v10, v193
	v_mov_b32_e32 v11, v193
	v_mov_b32_e32 v12, v193
	v_mov_b32_e32 v13, v193
	v_mov_b64_e32 v[30:31], v[14:15]
	v_mov_b64_e32 v[46:47], v[14:15]
	v_mov_b64_e32 v[62:63], v[14:15]
	s_or_b32 s16, s4, 64
	v_mov_b64_e32 v[28:29], v[12:13]
	v_mov_b64_e32 v[26:27], v[10:11]
	v_mov_b64_e32 v[24:25], v[8:9]
	v_mov_b64_e32 v[22:23], v[6:7]
	v_mov_b64_e32 v[20:21], v[4:5]
	v_mov_b64_e32 v[18:19], v[2:3]
	v_mov_b64_e32 v[16:17], v[0:1]
	v_mov_b64_e32 v[44:45], v[12:13]
	v_mov_b64_e32 v[42:43], v[10:11]
	v_mov_b64_e32 v[40:41], v[8:9]
	v_mov_b64_e32 v[38:39], v[6:7]
	v_mov_b64_e32 v[36:37], v[4:5]
	v_mov_b64_e32 v[34:35], v[2:3]
	v_mov_b64_e32 v[32:33], v[0:1]
	v_mov_b64_e32 v[60:61], v[12:13]
	v_mov_b64_e32 v[58:59], v[10:11]
	v_mov_b64_e32 v[56:57], v[8:9]
	v_mov_b64_e32 v[54:55], v[6:7]
	v_mov_b64_e32 v[52:53], v[4:5]
	v_mov_b64_e32 v[50:51], v[2:3]
	v_mov_b64_e32 v[48:49], v[0:1]
	s_waitcnt vmcnt(0) lgkmcnt(0)
	s_barrier
	s_and_b32 s30, s28, 1
	s_cmp_eq_u32 s28, 63
	s_cbranch_scc1 .LBB0_788
	s_branch .LBB0_787

; #define SBAR() __builtin_amdgcn_sched_barrier(0)
; template <int MODE>
; __device__ __forceinline__ void partialSM(f32x16& p0, f32x16& p1, float& m_reg, float& mn, float& alpha) {
;     ...
;     const float mnC = -mn * C;
; #pragma unroll
;     for (int r = 0; r < 16; ++r) p0[r] = fmaf(p0[r], C, mnC);
; #pragma unroll
;     for (int r = 0; r < 16; ++r) p1[r] = fmaf(p1[r], C, mnC);
; #pragma unroll
;     for (int r = 0; r < 16; ++r) p0[r] = __builtin_amdgcn_exp2f(p0[r]);
; }
; __device__ __forceinline__ void finishSM(f32x16& p0, f32x16& p1, float alpha, float& l_reg, bf16x8& pa0, bf16x8& pa1, bf16x8& pa2, bf16x8& pa3) {
; #pragma unroll
;     for (int r = 0; r < 16; ++r) p1[r] = __builtin_amdgcn_exp2f(p1[r]);
;     float ps = 0;
; #pragma unroll
;     for (int r = 0; r < 16; ++r) ps += p0[r];
; #pragma unroll
;     for (int r = 0; r < 16; ++r) ps += p1[r];
;     { auto rr = __builtin_amdgcn_permlane32_swap(__float_as_uint(ps), __float_as_uint(ps), false, false);
;       ps = __uint_as_float(rr[0]) + __uint_as_float(rr[1]); }
;     l_reg = l_reg * alpha + ps;
;     ...
;     PK4(p0, 0, pa0); PK4(p0, 8, pa1); PK4(p1, 0, pa2); PK4(p1, 8, pa3);
;     ...
; }
; template <int D0> __device__ __forceinline__ void pv_one(f32x16& od, int vb, bf16x8 pa0, bf16x8 pa1, bf16x8 pa2, bf16x8 pa3) {
;     const s16x4 l0 = tr_read<v_rd_off(D0, 0, 0)>(vb), h0 = tr_read<v_rd_off(D0, 0, 1)>(vb), l1 = tr_read<v_rd_off(D0, 1, 0)>(vb), h1 = tr_read<v_rd_off(D0, 1, 1)>(vb);
;     const s16x4 l2 = tr_read<v_rd_off(D0, 2, 0)>(vb), h2 = tr_read<v_rd_off(D0, 2, 1)>(vb), l3 = tr_read<v_rd_off(D0, 3, 0)>(vb), h3 = tr_read<v_rd_off(D0, 3, 1)>(vb);
;     asm volatile("s_waitcnt lgkmcnt(0)" ::: "memory"); SBAR();
;     ...
;     od = __builtin_amdgcn_mfma_f32_32x32x16_bf16(pa0, PK(l0, h0), od, 0, 0, 0);
;     od = __builtin_amdgcn_mfma_f32_32x32x16_bf16(pa1, PK(l1, h1), od, 0, 0, 0);
;     od = __builtin_amdgcn_mfma_f32_32x32x16_bf16(pa2, PK(l2, h2), od, 0, 0, 0);
;     od = __builtin_amdgcn_mfma_f32_32x32x16_bf16(pa3, PK(l3, h3), od, 0, 0, 0);
;     ...
; }
; __device__ __forceinline__ void pv_d0(f32x16* o, int vb, bf16x8 pa0, bf16x8 pa1, bf16x8 pa2, bf16x8 pa3) {
;     pv_one<0>(o[0], vb, pa0, pa1, pa2, pa3); pv_one<1>(o[1], vb, pa0, pa1, pa2, pa3); pv_one<2>(o[2], vb, pa0, pa1, pa2, pa3); pv_one<3>(o[3], vb, pa0, pa1, pa2, pa3);
.LBB0_792:
	v_cndmask_b32_e64 v173, v176, v173, s[4:5]
	v_mul_f32_e32 v176, 0xbdd53b94, v173
	v_fmamk_f32 v80, v80, 0x3dd53b94, v176
	v_fmamk_f32 v81, v81, 0x3dd53b94, v176
	v_fmamk_f32 v82, v82, 0x3dd53b94, v176
	v_fmamk_f32 v83, v83, 0x3dd53b94, v176
	v_fmamk_f32 v84, v84, 0x3dd53b94, v176
	v_fmamk_f32 v85, v85, 0x3dd53b94, v176
	v_fmamk_f32 v86, v86, 0x3dd53b94, v176
	v_fmamk_f32 v87, v87, 0x3dd53b94, v176
	v_fmamk_f32 v88, v88, 0x3dd53b94, v176
	v_fmamk_f32 v89, v89, 0x3dd53b94, v176
	v_fmamk_f32 v90, v90, 0x3dd53b94, v176
	v_fmamk_f32 v91, v91, 0x3dd53b94, v176
	v_fmamk_f32 v92, v92, 0x3dd53b94, v176
	v_fmamk_f32 v93, v93, 0x3dd53b94, v176
	v_fmamk_f32 v94, v94, 0x3dd53b94, v176
	v_fmamk_f32 v95, v95, 0x3dd53b94, v176
	v_fmamk_f32 v64, v64, 0x3dd53b94, v176
	v_fmamk_f32 v65, v65, 0x3dd53b94, v176
	v_fmamk_f32 v66, v66, 0x3dd53b94, v176
	v_fmamk_f32 v67, v67, 0x3dd53b94, v176
	v_fmamk_f32 v68, v68, 0x3dd53b94, v176
	v_fmamk_f32 v69, v69, 0x3dd53b94, v176
	v_fmamk_f32 v70, v70, 0x3dd53b94, v176
	v_fmamk_f32 v71, v71, 0x3dd53b94, v176
	v_fmamk_f32 v72, v72, 0x3dd53b94, v176
	v_fmamk_f32 v73, v73, 0x3dd53b94, v176
	v_fmamk_f32 v74, v74, 0x3dd53b94, v176
	v_fmamk_f32 v75, v75, 0x3dd53b94, v176
	v_fmamk_f32 v76, v76, 0x3dd53b94, v176
	v_fmamk_f32 v77, v77, 0x3dd53b94, v176
	v_fmamk_f32 v78, v78, 0x3dd53b94, v176
	v_fmac_f32_e32 v176, 0x3dd53b94, v79
	v_exp_f32_e32 v79, v80
	v_exp_f32_e32 v80, v81
	v_exp_f32_e32 v81, v82
	v_exp_f32_e32 v82, v83
	v_exp_f32_e32 v83, v84
	v_exp_f32_e32 v84, v85
	v_exp_f32_e32 v85, v86
	v_exp_f32_e32 v86, v87
	v_exp_f32_e32 v87, v88
	v_exp_f32_e32 v88, v89
	v_exp_f32_e32 v89, v90
	v_exp_f32_e32 v90, v91
	v_exp_f32_e32 v91, v92
	v_exp_f32_e32 v92, v93
	v_exp_f32_e32 v93, v94
	v_exp_f32_e32 v94, v95
	v_exp_f32_e32 v95, v64
	v_add_f32_e32 v64, 0, v79
	v_add_f32_e32 v64, v80, v64
	v_add_f32_e32 v64, v81, v64
	v_add_f32_e32 v64, v82, v64
	v_add_f32_e32 v64, v83, v64
	v_add_f32_e32 v64, v84, v64
	v_add_f32_e32 v64, v85, v64
	v_add_f32_e32 v64, v86, v64
	v_add_f32_e32 v64, v87, v64
	v_add_f32_e32 v64, v88, v64
	v_add_f32_e32 v64, v89, v64
	v_add_f32_e32 v64, v90, v64
	v_add_f32_e32 v64, v91, v64
	v_exp_f32_e32 v65, v65
	v_add_f32_e32 v64, v92, v64
	v_exp_f32_e32 v177, v66
	v_add_f32_e32 v64, v93, v64
	v_exp_f32_e32 v178, v67
	v_add_f32_e32 v64, v94, v64
	v_exp_f32_e32 v179, v68
	v_add_f32_e32 v64, v95, v64
	v_exp_f32_e32 v180, v69
	v_add_f32_e32 v64, v65, v64
	v_exp_f32_e32 v181, v70
	v_add_f32_e32 v64, v177, v64
	v_exp_f32_e32 v182, v71
	v_add_f32_e32 v64, v178, v64
	v_exp_f32_e32 v183, v72
	v_add_f32_e32 v64, v179, v64
	v_exp_f32_e32 v184, v73
	v_add_f32_e32 v64, v180, v64
	v_exp_f32_e32 v185, v74
	v_add_f32_e32 v64, v181, v64
	v_exp_f32_e32 v186, v75
	v_add_f32_e32 v64, v182, v64
	v_exp_f32_e32 v187, v76
	v_add_f32_e32 v64, v183, v64
	v_exp_f32_e32 v188, v77
	v_add_f32_e32 v64, v184, v64
	v_exp_f32_e32 v189, v78
	v_add_f32_e32 v64, v185, v64
	v_exp_f32_e32 v176, v176
	v_add_f32_e32 v64, v186, v64
	v_add_f32_e32 v64, v187, v64
	v_add_f32_e32 v64, v188, v64
	v_add_f32_e32 v64, v189, v64
	v_add_f32_e32 v64, v176, v64
	v_mov_b32_e32 v66, v64
	s_nop 1
	v_permlane32_swap_b32_e32 v64, v66
	v_add_f32_e32 v64, v64, v66
	s_add_i32 s28, s28, 1
	v_fmac_f32_e32 v64, v174, v175
	v_cvt_pk_bf16_f32 v66, v79, v80
	v_cvt_pk_bf16_f32 v67, v81, v82
	v_cvt_pk_bf16_f32 v68, v83, v84
	v_cvt_pk_bf16_f32 v69, v85, v86
	v_cvt_pk_bf16_f32 v70, v87, v88
	v_cvt_pk_bf16_f32 v71, v89, v90
	v_cvt_pk_bf16_f32 v72, v91, v92
	v_cvt_pk_bf16_f32 v73, v93, v94
	v_cvt_pk_bf16_f32 v74, v95, v65
	v_cvt_pk_bf16_f32 v75, v177, v178
	v_cvt_pk_bf16_f32 v76, v179, v180
	v_cvt_pk_bf16_f32 v77, v181, v182
	v_cvt_pk_bf16_f32 v78, v183, v184
	v_cvt_pk_bf16_f32 v79, v185, v186
	v_cvt_pk_bf16_f32 v80, v187, v188
	v_cvt_pk_bf16_f32 v81, v189, v176
	s_nop 0
	v_permlane32_swap_b32_e32 v66, v68
	v_permlane32_swap_b32_e32 v67, v69
	v_permlane32_swap_b32_e32 v70, v72
	v_permlane32_swap_b32_e32 v71, v73
	v_permlane32_swap_b32_e32 v74, v76
	v_permlane32_swap_b32_e32 v75, v77
	v_permlane32_swap_b32_e32 v78, v80
	v_permlane32_swap_b32_e32 v79, v81
	v_lshl_add_u32 v65, s30, 14, v172
	ds_read_b64_tr_b16 v[82:83], v65 offset:0
	ds_read_b64_tr_b16 v[84:85], v65 offset:0x800
	ds_read_b64_tr_b16 v[86:87], v65 offset:0x1000
	ds_read_b64_tr_b16 v[88:89], v65 offset:0x1800
	ds_read_b64_tr_b16 v[90:91], v65 offset:0x2000
	ds_read_b64_tr_b16 v[92:93], v65 offset:0x2800
	ds_read_b64_tr_b16 v[174:175], v65 offset:0x3000
	ds_read_b64_tr_b16 v[176:177], v65 offset:0x3800
	s_waitcnt lgkmcnt(0)
	s_nop 0
	v_mfma_f32_32x32x16_bf16 v[0:15], v[66:69], v[82:85], v[0:15]
	ds_read_b64_tr_b16 v[82:83], v65 offset:0x200
	ds_read_b64_tr_b16 v[84:85], v65 offset:0xa00
	v_mfma_f32_32x32x16_bf16 v[0:15], v[70:73], v[86:89], v[0:15]
	ds_read_b64_tr_b16 v[86:87], v65 offset:0x1200
	ds_read_b64_tr_b16 v[88:89], v65 offset:0x1a00
	v_mfma_f32_32x32x16_bf16 v[0:15], v[74:77], v[90:93], v[0:15]
	ds_read_b64_tr_b16 v[90:91], v65 offset:0x2200
	ds_read_b64_tr_b16 v[92:93], v65 offset:0x2a00
	v_mfma_f32_32x32x16_bf16 v[0:15], v[78:81], v[174:177], v[0:15]
	ds_read_b64_tr_b16 v[174:175], v65 offset:0x3200
	ds_read_b64_tr_b16 v[176:177], v65 offset:0x3a00
	s_waitcnt lgkmcnt(0)
	v_mfma_f32_32x32x16_bf16 v[16:31], v[66:69], v[82:85], v[16:31]
	ds_read_b64_tr_b16 v[82:83], v65 offset:0x400
	ds_read_b64_tr_b16 v[84:85], v65 offset:0xc00
	v_mfma_f32_32x32x16_bf16 v[16:31], v[70:73], v[86:89], v[16:31]
	ds_read_b64_tr_b16 v[86:87], v65 offset:0x1400
	ds_read_b64_tr_b16 v[88:89], v65 offset:0x1c00
	v_mfma_f32_32x32x16_bf16 v[16:31], v[74:77], v[90:93], v[16:31]
	ds_read_b64_tr_b16 v[90:91], v65 offset:0x2400
	ds_read_b64_tr_b16 v[92:93], v65 offset:0x2c00
	v_mfma_f32_32x32x16_bf16 v[16:31], v[78:81], v[174:177], v[16:31]
	ds_read_b64_tr_b16 v[174:175], v65 offset:0x3400
	ds_read_b64_tr_b16 v[176:177], v65 offset:0x3c00
	s_waitcnt lgkmcnt(0)
	v_mfma_f32_32x32x16_bf16 v[32:47], v[66:69], v[82:85], v[32:47]
	ds_read_b64_tr_b16 v[82:83], v65 offset:0x600
	ds_read_b64_tr_b16 v[84:85], v65 offset:0xe00
	v_mfma_f32_32x32x16_bf16 v[32:47], v[70:73], v[86:89], v[32:47]
	ds_read_b64_tr_b16 v[86:87], v65 offset:0x1600
	ds_read_b64_tr_b16 v[88:89], v65 offset:0x1e00
	v_mfma_f32_32x32x16_bf16 v[32:47], v[74:77], v[90:93], v[32:47]
	ds_read_b64_tr_b16 v[90:91], v65 offset:0x2600
	ds_read_b64_tr_b16 v[92:93], v65 offset:0x2e00
	v_mfma_f32_32x32x16_bf16 v[32:47], v[78:81], v[174:177], v[32:47]
	ds_read_b64_tr_b16 v[174:175], v65 offset:0x3600
	ds_read_b64_tr_b16 v[176:177], v65 offset:0x3e00
	s_waitcnt lgkmcnt(0)
	v_mfma_f32_32x32x16_bf16 v[48:63], v[66:69], v[82:85], v[48:63]
	s_waitcnt vmcnt(0)
	s_add_i32 s16, s16, 64
	s_cmp_eq_u32 s28, 64
	s_waitcnt vmcnt(0)
	s_barrier
	v_mfma_f32_32x32x16_bf16 v[48:63], v[70:73], v[86:89], v[48:63]
	v_mfma_f32_32x32x16_bf16 v[48:63], v[74:77], v[90:93], v[48:63]
	v_mfma_f32_32x32x16_bf16 v[48:63], v[78:81], v[174:177], v[48:63]
	s_cbranch_scc0 .LBB0_786
	s_setprio 0
	s_and_saveexec_b64 s[0:1], s[2:3]
	s_cbranch_execz .LBB0_784
	ds_write_b32 v163, v64
	s_branch .LBB0_784
